# v52 + k_readout: WbT staged in LDS cooperatively (each wave loads a quarter, one barrier), mat-vec reads LDS
# baseline (speedup 1.0000x reference)
_Z9k_readoutPKDv4_jPKfPKiPK15HIP_vector_typeIiLj2EES3_S3_S3_PfSA_:
	s_load_dwordx4 s[4:7], s[0:1], 0x0
	s_load_dwordx2 s[8:9], s[0:1], 0x10
	s_load_dwordx2 s[12:13], s[0:1], 0x18
	s_load_dwordx2 s[14:15], s[0:1], 0x28
	v_lshrrev_b32_e32 v53, 6, v0
	v_lshl_or_b32 v44, s2, 2, v53
	v_ashrrev_i32_e32 v45, 31, v44
	v_and_b32_e32 v52, 63, v0
	s_waitcnt lgkmcnt(0)
	v_lshl_add_u64 v[2:3], v[44:45], 2, s[8:9]
	global_load_dword v57, v[2:3], off
	v_mov_b32_e32 v9, 0
	v_lshlrev_b64 v[2:3], 8, v[44:45]
	v_lshl_add_u64 v[2:3], s[6:7], 0, v[2:3]
	v_lshlrev_b32_e32 v46, 2, v52
	v_mov_b32_e32 v47, v9
	v_lshl_add_u64 v[2:3], v[2:3], 0, v[46:47]
	v_add_co_u32_e32 v4, vcc, 0x200000, v2
	s_load_dwordx2 s[6:7], s[0:1], 0x30
	s_nop 0
	v_addc_co_u32_e32 v5, vcc, 0, v3, vcc
	global_load_dword v48, v[2:3], off
	global_load_dword v49, v[4:5], off
	v_lshlrev_b64 v[10:11], 10, v[44:45]
	v_lshl_add_u64 v[10:11], s[12:13], 0, v[10:11]
	v_lshlrev_b32_e32 v12, 3, v52
	v_mov_b32_e32 v13, 0
	v_lshl_add_u64 v[10:11], v[10:11], 0, v[12:13]
	global_load_dwordx2 v[24:25], v[10:11], off
	v_lshlrev_b32_e32 v60, 4, v52
	v_lshl_or_b32 v60, v53, 12, v60
	global_load_dwordx4 v[64:67], v60, s[14:15]
	global_load_dwordx4 v[68:71], v60, s[14:15] offset:1024
	global_load_dwordx4 v[72:75], v60, s[14:15] offset:2048
	global_load_dwordx4 v[76:79], v60, s[14:15] offset:3072
	v_bfe_u32 v54, v0, 5, 1
	s_waitcnt lgkmcnt(0)
	s_load_dword s2, s[6:7], 0x0
	s_movk_i32 s6, 0x80
	v_and_b32_e32 v47, 7, v0
	v_lshlrev_b32_e32 v8, 20, v54
	s_mov_b32 s3, 0
	v_bfe_u32 v55, v0, 3, 2
	v_mbcnt_lo_u32_b32 v56, -1, 0
	s_waitcnt vmcnt(7)
	v_cmp_lt_i32_e32 vcc, s6, v57
	s_and_saveexec_b64 s[6:7], vcc
	s_xor_b64 s[6:7], exec, s[6:7]
	s_cbranch_execz .LBB4_10
	s_waitcnt vmcnt(0)
	v_add_u32_e32 v61, 0x1800, v60
	ds_write_b128 v61, v[64:67]
	ds_write_b128 v61, v[68:71] offset:1024
	ds_write_b128 v61, v[72:75] offset:2048
	ds_write_b128 v61, v[76:79] offset:3072
	s_load_dwordx2 s[8:9], s[0:1], 0x20
	v_lshl_add_u64 v[0:1], s[4:5], 0, v[8:9]
	v_lshlrev_b32_e32 v8, 4, v47
	v_lshlrev_b64 v[2:3], 15, v[44:45]
	v_lshl_add_u64 v[16:17], v[0:1], 0, v[8:9]
	v_mbcnt_hi_u32_b32 v1, -1, v56
	s_waitcnt lgkmcnt(0)
	v_lshl_add_u64 v[18:19], s[8:9], 0, v[2:3]
	v_lshlrev_b32_e32 v0, 2, v55
	v_mov_b32_e32 v8, v9
	v_lshlrev_b32_e32 v1, 2, v1
	s_movk_i32 s8, 0x100
	v_mov_b32_e32 v10, v9
	v_mov_b32_e32 v11, v9
	v_mov_b32_e32 v12, v9
	v_mov_b32_e32 v13, v9
	v_mov_b32_e32 v14, v9
	v_mov_b32_e32 v15, v9
	v_and_or_b32 v23, v1, s8, v0
	v_mov_b64_e32 v[0:1], v[8:9]
	v_mov_b32_e32 v22, 0
	v_mov_b64_e32 v[2:3], v[10:11]
	v_mov_b64_e32 v[4:5], v[12:13]
	v_mov_b64_e32 v[6:7], v[14:15]

.LBB4_13:
	s_or_b64 exec, exec, s[8:9]
	v_lshlrev_b32_e32 v58, 9, v53
	v_cmp_lt_i32_e32 vcc, v52, v57
	v_or_b32_e32 v1, 0x800, v58
	v_or_b32_e32 v2, v1, v46
	s_waitcnt vmcnt(0)
	v_add_u32_e32 v61, 0x1800, v60
	ds_write_b128 v61, v[64:67]
	ds_write_b128 v61, v[68:71] offset:1024
	ds_write_b128 v61, v[72:75] offset:2048
	ds_write_b128 v61, v[76:79] offset:3072
	v_cndmask_b32_e32 v0, v44, v24, vcc
	ds_write2st64_b32 v2, v0, v50 offset1:1
	v_lshlrev_b32_e32 v50, 2, v55
	v_or_b32_e32 v26, v1, v50
	ds_read2_b32 v[0:1], v26 offset1:4
	ds_read2_b32 v[20:21], v26 offset0:16 offset1:20
	v_lshl_or_b32 v45, v47, 4, v8
	v_cndmask_b32_e32 v59, 0, v25, vcc
	ds_read2_b32 v[24:25], v26 offset0:24 offset1:28
	s_waitcnt lgkmcnt(2)
	v_lshl_add_u32 v0, v0, 7, v45
	s_waitcnt lgkmcnt(1)
	v_lshl_add_u32 v16, v20, 7, v45
	global_load_dwordx4 v[8:11], v0, s[4:5]
	v_lshl_add_u32 v20, v21, 7, v45
	global_load_dwordx4 v[16:19], v16, s[4:5]
	v_lshl_add_u32 v0, v1, 7, v45
	global_load_dwordx4 v[12:15], v0, s[4:5]
	v_or_b32_e32 v27, 0x1000, v58
	global_load_dwordx4 v[20:23], v20, s[4:5]
	ds_read2_b32 v[0:1], v26 offset0:8 offset1:12
	s_waitcnt lgkmcnt(1)
	v_lshl_add_u32 v24, v24, 7, v45
	v_or_b32_e32 v30, v27, v46
	v_or_b32_e32 v60, v27, v50
	s_mov_b32 s3, 48
	s_waitcnt lgkmcnt(0)
	v_lshl_add_u32 v0, v0, 7, v45
	global_load_dwordx4 v[4:7], v0, s[4:5]
	v_lshl_add_u32 v0, v1, 7, v45
	global_load_dwordx4 v[0:3], v0, s[4:5]
	ds_read2_b32 v[28:29], v26 offset0:32 offset1:36
	ds_read2_b32 v[26:27], v26 offset0:40 offset1:44
	global_load_dwordx4 v[40:43], v24, s[4:5]
	ds_write2st64_b32 v30, v59, v51 offset1:1
	v_lshl_add_u32 v24, v25, 7, v45
	s_waitcnt lgkmcnt(2)
	v_lshl_add_u32 v25, v28, 7, v45
	v_lshl_add_u32 v28, v29, 7, v45
	s_waitcnt lgkmcnt(1)
	v_lshl_add_u32 v26, v26, 7, v45
	v_lshl_add_u32 v27, v27, 7, v45
	global_load_dwordx4 v[62:65], v24, s[4:5]
	global_load_dwordx4 v[36:39], v25, s[4:5]
	global_load_dwordx4 v[32:35], v28, s[4:5]
	s_nop 0
	global_load_dwordx4 v[28:31], v26, s[4:5]
	s_nop 0
	global_load_dwordx4 v[24:27], v27, s[4:5]
	v_cmp_lt_i32_e32 vcc, 48, v57
	s_waitcnt vmcnt(11)
	v_cvt_f32_f16_e32 v70, v10
	v_cvt_f32_f16_sdwa v71, v10 dst_sel:DWORD dst_unused:UNUSED_PAD src0_sel:WORD_1
	v_cvt_f32_f16_e32 v66, v8
	v_cvt_f32_f16_sdwa v67, v8 dst_sel:DWORD dst_unused:UNUSED_PAD src0_sel:WORD_1
	s_waitcnt vmcnt(9)
	v_cvt_f32_f16_e32 v74, v14
	v_cvt_f32_f16_sdwa v75, v14 dst_sel:DWORD dst_unused:UNUSED_PAD src0_sel:WORD_1
	s_waitcnt vmcnt(8)
	v_cvt_f32_f16_e32 v84, v22
	v_cvt_f32_f16_sdwa v85, v22 dst_sel:DWORD dst_unused:UNUSED_PAD src0_sel:WORD_1
	v_cvt_f32_f16_e32 v91, v23
	v_cvt_f32_f16_e32 v87, v15
	v_cvt_f32_f16_e32 v68, v9
	v_cvt_f32_f16_sdwa v69, v9 dst_sel:DWORD dst_unused:UNUSED_PAD src0_sel:WORD_1
	v_cvt_f32_f16_e32 v72, v12
	v_cvt_f32_f16_sdwa v73, v12 dst_sel:DWORD dst_unused:UNUSED_PAD src0_sel:WORD_1
	v_cvt_f32_f16_e32 v12, v13
	s_waitcnt vmcnt(6)
	v_cvt_f32_f16_e32 v78, v1
	v_cvt_f32_f16_sdwa v79, v1 dst_sel:DWORD dst_unused:UNUSED_PAD src0_sel:WORD_1
	v_cvt_f32_f16_sdwa v1, v23 dst_sel:DWORD dst_unused:UNUSED_PAD src0_sel:WORD_1
	ds_read2_b32 v[22:23], v60 offset1:4
	v_cvt_f32_f16_sdwa v13, v13 dst_sel:DWORD dst_unused:UNUSED_PAD src0_sel:WORD_1
	v_cvt_f32_f16_e32 v61, v11
	v_cvt_f32_f16_sdwa v9, v15 dst_sel:DWORD dst_unused:UNUSED_PAD src0_sel:WORD_1
	v_cvt_f32_f16_sdwa v8, v11 dst_sel:DWORD dst_unused:UNUSED_PAD src0_sel:WORD_1
	s_waitcnt lgkmcnt(0)
	v_mov_b32_e32 v86, v23
	v_pk_fma_f32 v[70:71], v[22:23], v[70:71], 0 op_sel_hi:[0,1,0]
	v_pk_fma_f32 v[70:71], v[86:87], v[74:75], v[70:71] op_sel_hi:[0,1,1]
	ds_read2_b32 v[74:75], v60 offset0:8 offset1:12
	v_cvt_f32_f16_e32 v10, v4
	v_cvt_f32_f16_sdwa v11, v4 dst_sel:DWORD dst_unused:UNUSED_PAD src0_sel:WORD_1
	v_cvt_f32_f16_e32 v14, v5
	v_cvt_f32_f16_sdwa v15, v5 dst_sel:DWORD dst_unused:UNUSED_PAD src0_sel:WORD_1
	v_cvt_f32_f16_e32 v76, v6
	v_cvt_f32_f16_sdwa v77, v6 dst_sel:DWORD dst_unused:UNUSED_PAD src0_sel:WORD_1
	v_cvt_f32_f16_e32 v88, v7
	v_cvt_f32_f16_sdwa v4, v7 dst_sel:DWORD dst_unused:UNUSED_PAD src0_sel:WORD_1
	v_cvt_f32_f16_e32 v6, v0
	v_cvt_f32_f16_sdwa v7, v0 dst_sel:DWORD dst_unused:UNUSED_PAD src0_sel:WORD_1
	v_cvt_f32_f16_e32 v80, v2
	v_cvt_f32_f16_sdwa v81, v2 dst_sel:DWORD dst_unused:UNUSED_PAD src0_sel:WORD_1
	v_pk_fma_f32 v[68:69], v[22:23], v[68:69], 0 op_sel_hi:[0,1,0]
	v_pk_fma_f32 v[66:67], v[22:23], v[66:67], 0 op_sel_hi:[0,1,0]
	v_pk_fma_f32 v[12:13], v[86:87], v[12:13], v[68:69] op_sel_hi:[0,1,1]
	v_pk_fma_f32 v[66:67], v[86:87], v[72:73], v[66:67] op_sel_hi:[0,1,1]
	s_waitcnt lgkmcnt(0)
	v_pk_fma_f32 v[10:11], v[74:75], v[10:11], v[66:67] op_sel_hi:[0,1,1]
	v_pk_fma_f32 v[12:13], v[74:75], v[14:15], v[12:13] op_sel_hi:[0,1,1]
	v_mov_b32_e32 v14, v75
	v_pk_fma_f32 v[66:67], v[74:75], v[76:77], v[70:71] op_sel_hi:[0,1,1]
	v_pk_fma_f32 v[66:67], v[14:15], v[80:81], v[66:67] op_sel_hi:[0,1,1]
	v_pk_fma_f32 v[12:13], v[14:15], v[78:79], v[12:13] op_sel_hi:[0,1,1]
	v_pk_fma_f32 v[6:7], v[14:15], v[6:7], v[10:11] op_sel_hi:[0,1,1]
	s_waitcnt vmcnt(5)
	v_cvt_f32_f16_e32 v10, v40
	v_cvt_f32_f16_sdwa v11, v40 dst_sel:DWORD dst_unused:UNUSED_PAD src0_sel:WORD_1
	v_cvt_f32_f16_e32 v14, v41
	v_cvt_f32_f16_sdwa v15, v41 dst_sel:DWORD dst_unused:UNUSED_PAD src0_sel:WORD_1
	ds_read2_b32 v[40:41], v60 offset0:16 offset1:20
	v_cvt_f32_f16_e32 v89, v3
	v_cvt_f32_f16_sdwa v5, v3 dst_sel:DWORD dst_unused:UNUSED_PAD src0_sel:WORD_1
	v_cvt_f32_f16_e32 v2, v16
	v_cvt_f32_f16_sdwa v3, v16 dst_sel:DWORD dst_unused:UNUSED_PAD src0_sel:WORD_1
	v_cvt_f32_f16_e32 v16, v17
	v_cvt_f32_f16_sdwa v17, v17 dst_sel:DWORD dst_unused:UNUSED_PAD src0_sel:WORD_1
	v_cvt_f32_f16_e32 v90, v19
	v_cvt_f32_f16_e32 v82, v18
	v_cvt_f32_f16_sdwa v83, v18 dst_sel:DWORD dst_unused:UNUSED_PAD src0_sel:WORD_1
	v_cvt_f32_f16_sdwa v0, v19 dst_sel:DWORD dst_unused:UNUSED_PAD src0_sel:WORD_1
	v_cvt_f32_f16_e32 v18, v20
	v_cvt_f32_f16_sdwa v19, v20 dst_sel:DWORD dst_unused:UNUSED_PAD src0_sel:WORD_1
	v_cvt_f32_f16_e32 v20, v21
	v_cvt_f32_f16_sdwa v21, v21 dst_sel:DWORD dst_unused:UNUSED_PAD src0_sel:WORD_1
	s_waitcnt lgkmcnt(0)
	v_pk_fma_f32 v[2:3], v[40:41], v[2:3], v[6:7] op_sel_hi:[0,1,1]
	v_pk_fma_f32 v[6:7], v[40:41], v[16:17], v[12:13] op_sel_hi:[0,1,1]
	v_mov_b32_e32 v16, v41
	v_pk_fma_f32 v[2:3], v[16:17], v[18:19], v[2:3] op_sel_hi:[0,1,1]
	ds_read2_b32 v[18:19], v60 offset0:24 offset1:28
	v_cvt_f32_f16_e32 v68, v42
	v_cvt_f32_f16_sdwa v69, v42 dst_sel:DWORD dst_unused:UNUSED_PAD src0_sel:WORD_1
	v_pk_fma_f32 v[12:13], v[40:41], v[82:83], v[66:67] op_sel_hi:[0,1,1]
	v_pk_fma_f32 v[12:13], v[16:17], v[84:85], v[12:13] op_sel_hi:[0,1,1]
	v_pk_fma_f32 v[6:7], v[16:17], v[20:21], v[6:7] op_sel_hi:[0,1,1]
	s_waitcnt vmcnt(4)
	v_cvt_f32_f16_e32 v20, v62
	v_cvt_f32_f16_sdwa v21, v62 dst_sel:DWORD dst_unused:UNUSED_PAD src0_sel:WORD_1
	v_cvt_f32_f16_e32 v16, v63
	v_cvt_f32_f16_sdwa v17, v63 dst_sel:DWORD dst_unused:UNUSED_PAD src0_sel:WORD_1
	v_cvt_f32_f16_e32 v62, v64
	v_cvt_f32_f16_sdwa v63, v64 dst_sel:DWORD dst_unused:UNUSED_PAD src0_sel:WORD_1
	v_pk_mul_f32 v[8:9], v[22:23], v[8:9]
	s_waitcnt lgkmcnt(0)
	v_pk_fma_f32 v[2:3], v[18:19], v[10:11], v[2:3] op_sel_hi:[0,1,1]
	v_pk_fma_f32 v[10:11], v[18:19], v[68:69], v[12:13] op_sel_hi:[0,1,1]
	v_mov_b32_e32 v12, v19
	s_waitcnt vmcnt(0)
	v_cvt_f32_f16_e32 v66, v26
	v_cvt_f32_f16_sdwa v67, v26 dst_sel:DWORD dst_unused:UNUSED_PAD src0_sel:WORD_1
	v_mul_f32_e32 v22, v22, v61
	v_mul_f32_e32 v26, v23, v87
	v_mov_b32_e32 v23, v8
	v_pk_fma_f32 v[10:11], v[12:13], v[62:63], v[10:11] op_sel_hi:[0,1,1]
	v_cvt_f32_f16_e32 v62, v30
	v_cvt_f32_f16_sdwa v63, v30 dst_sel:DWORD dst_unused:UNUSED_PAD src0_sel:WORD_1
	v_cvt_f32_f16_e32 v72, v31
	v_cvt_f32_f16_sdwa v30, v31 dst_sel:DWORD dst_unused:UNUSED_PAD src0_sel:WORD_1
	v_cvt_f32_f16_sdwa v31, v27 dst_sel:DWORD dst_unused:UNUSED_PAD src0_sel:WORD_1
	v_cvt_f32_f16_e32 v73, v27
	v_mov_b32_e32 v27, v9
	v_pk_add_f32 v[8:9], v[22:23], 0 op_sel_hi:[1,0]
	v_pk_mul_f32 v[4:5], v[74:75], v[4:5]
	v_pk_add_f32 v[8:9], v[8:9], v[26:27]
	v_mul_f32_e32 v22, v74, v88
	v_mov_b32_e32 v23, v4
	v_pk_add_f32 v[8:9], v[8:9], v[22:23]
	v_mul_f32_e32 v4, v75, v89
	v_pk_mul_f32 v[0:1], v[40:41], v[0:1]
	v_pk_add_f32 v[4:5], v[8:9], v[4:5]
	v_mul_f32_e32 v8, v40, v90
	v_mov_b32_e32 v9, v0
	v_pk_add_f32 v[4:5], v[4:5], v[8:9]
	v_mul_f32_e32 v0, v41, v91
	v_pk_fma_f32 v[6:7], v[18:19], v[14:15], v[6:7] op_sel_hi:[0,1,1]
	v_pk_add_f32 v[0:1], v[4:5], v[0:1]
	ds_read2_b32 v[4:5], v60 offset0:32 offset1:36
	v_pk_fma_f32 v[6:7], v[12:13], v[16:17], v[6:7] op_sel_hi:[0,1,1]
	v_pk_fma_f32 v[2:3], v[12:13], v[20:21], v[2:3] op_sel_hi:[0,1,1]
	v_cvt_f32_f16_e32 v12, v36
	v_cvt_f32_f16_sdwa v13, v36 dst_sel:DWORD dst_unused:UNUSED_PAD src0_sel:WORD_1
	v_cvt_f32_f16_e32 v70, v43
	v_cvt_f32_f16_sdwa v42, v43 dst_sel:DWORD dst_unused:UNUSED_PAD src0_sel:WORD_1
	v_cvt_f32_f16_sdwa v43, v65 dst_sel:DWORD dst_unused:UNUSED_PAD src0_sel:WORD_1
	v_cvt_f32_f16_e32 v71, v65
	v_cvt_f32_f16_sdwa v20, v39 dst_sel:DWORD dst_unused:UNUSED_PAD src0_sel:WORD_1
	v_cvt_f32_f16_sdwa v21, v35 dst_sel:DWORD dst_unused:UNUSED_PAD src0_sel:WORD_1
	v_cvt_f32_f16_e32 v14, v37
	v_cvt_f32_f16_sdwa v15, v37 dst_sel:DWORD dst_unused:UNUSED_PAD src0_sel:WORD_1
	v_cvt_f32_f16_e32 v68, v39
	s_waitcnt lgkmcnt(0)
	v_pk_fma_f32 v[2:3], v[4:5], v[12:13], v[2:3] op_sel_hi:[0,1,1]
	ds_read2_b32 v[12:13], v60 offset0:40 offset1:44
	v_cvt_f32_f16_e32 v16, v38
	v_cvt_f32_f16_sdwa v17, v38 dst_sel:DWORD dst_unused:UNUSED_PAD src0_sel:WORD_1
	v_cvt_f32_f16_e32 v69, v35
	v_pk_mul_f32 v[8:9], v[18:19], v[42:43]
	v_cvt_f32_f16_e32 v36, v32
	v_cvt_f32_f16_sdwa v37, v32 dst_sel:DWORD dst_unused:UNUSED_PAD src0_sel:WORD_1
	v_cvt_f32_f16_e32 v32, v33
	v_cvt_f32_f16_sdwa v33, v33 dst_sel:DWORD dst_unused:UNUSED_PAD src0_sel:WORD_1
	v_cvt_f32_f16_e32 v38, v34
	v_cvt_f32_f16_sdwa v39, v34 dst_sel:DWORD dst_unused:UNUSED_PAD src0_sel:WORD_1
	v_mul_f32_e32 v22, v18, v70
	v_mov_b32_e32 v23, v8
	v_cvt_f32_f16_e32 v34, v28
	v_cvt_f32_f16_sdwa v35, v28 dst_sel:DWORD dst_unused:UNUSED_PAD src0_sel:WORD_1
	v_cvt_f32_f16_e32 v28, v29
	v_cvt_f32_f16_sdwa v29, v29 dst_sel:DWORD dst_unused:UNUSED_PAD src0_sel:WORD_1
	v_pk_add_f32 v[0:1], v[0:1], v[22:23]
	v_mul_f32_e32 v8, v19, v71
	v_pk_mul_f32 v[18:19], v[4:5], v[20:21]
	v_cvt_f32_f16_e32 v64, v24
	v_cvt_f32_f16_sdwa v65, v24 dst_sel:DWORD dst_unused:UNUSED_PAD src0_sel:WORD_1
	v_cvt_f32_f16_e32 v24, v25
	v_cvt_f32_f16_sdwa v25, v25 dst_sel:DWORD dst_unused:UNUSED_PAD src0_sel:WORD_1
	v_pk_fma_f32 v[6:7], v[4:5], v[14:15], v[6:7] op_sel_hi:[0,1,1]
	v_mul_f32_e32 v14, v4, v68
	v_pk_add_f32 v[0:1], v[0:1], v[8:9]
	v_mov_b32_e32 v15, v18
	v_pk_fma_f32 v[10:11], v[4:5], v[16:17], v[10:11] op_sel_hi:[0,1,1]
	v_mul_f32_e32 v16, v5, v69
	v_mov_b32_e32 v20, v5
	s_waitcnt lgkmcnt(0)
	v_pk_mul_f32 v[26:27], v[12:13], v[30:31]
	v_pk_add_f32 v[0:1], v[0:1], v[14:15]
	v_mov_b32_e32 v17, v19
	v_mul_f32_e32 v4, v12, v72
	v_pk_fma_f32 v[10:11], v[20:21], v[38:39], v[10:11] op_sel_hi:[0,1,1]
	v_pk_fma_f32 v[6:7], v[20:21], v[32:33], v[6:7] op_sel_hi:[0,1,1]
	v_pk_fma_f32 v[2:3], v[20:21], v[36:37], v[2:3] op_sel_hi:[0,1,1]
	v_pk_add_f32 v[0:1], v[0:1], v[16:17]
	v_mov_b32_e32 v5, v26
	v_mov_b32_e32 v22, v13
	v_mul_f32_e32 v8, v13, v73
	v_pk_add_f32 v[14:15], v[0:1], v[4:5]
	v_pk_fma_f32 v[0:1], v[12:13], v[34:35], v[2:3] op_sel_hi:[0,1,1]
	v_pk_fma_f32 v[2:3], v[12:13], v[28:29], v[6:7] op_sel_hi:[0,1,1]
	v_pk_fma_f32 v[4:5], v[12:13], v[62:63], v[10:11] op_sel_hi:[0,1,1]
	v_mov_b32_e32 v9, v27
	v_pk_fma_f32 v[4:5], v[22:23], v[66:67], v[4:5] op_sel_hi:[0,1,1]
	v_pk_fma_f32 v[2:3], v[22:23], v[24:25], v[2:3] op_sel_hi:[0,1,1]
	v_pk_fma_f32 v[0:1], v[22:23], v[64:65], v[0:1] op_sel_hi:[0,1,1]
	v_pk_add_f32 v[6:7], v[14:15], v[8:9]
	s_and_saveexec_b64 s[8:9], vcc
	s_cbranch_execz .LBB4_17
	s_movk_i32 s10, 0x8c0
	v_or3_b32 v24, v58, v50, s10
	s_mov_b64 s[10:11], 0

.LBB4_20:
	s_or_b64 exec, exec, s[10:11]
	v_mov_b32_e32 v47, 0
	v_lshlrev_b32_e32 v0, 2, v52
	v_add_u32_e32 v0, 0x1800, v0
	s_waitcnt lgkmcnt(0)
	s_barrier
	s_mov_b64 s[0:1], 0
	v_mov_b32_e32 v46, v47

	.amdhsa_kernel _Z9k_readoutPKDv4_jPKfPKiPK15HIP_vector_typeIiLj2EES3_S3_S3_PfSA_
		.amdhsa_group_segment_fixed_size 22528
		.amdhsa_private_segment_fixed_size 0
		.amdhsa_kernarg_size 72
		.amdhsa_user_sgpr_count 2
		.amdhsa_user_sgpr_dispatch_ptr 0
		.amdhsa_user_sgpr_queue_ptr 0
		.amdhsa_user_sgpr_kernarg_segment_ptr 1
		.amdhsa_user_sgpr_dispatch_id 0
		.amdhsa_user_sgpr_kernarg_preload_length 0
		.amdhsa_user_sgpr_kernarg_preload_offset 0
		.amdhsa_user_sgpr_private_segment_size 0
		.amdhsa_uses_dynamic_stack 0
		.amdhsa_enable_private_segment 0
		.amdhsa_system_sgpr_workgroup_id_x 1
		.amdhsa_system_sgpr_workgroup_id_y 0
		.amdhsa_system_sgpr_workgroup_id_z 0
		.amdhsa_system_sgpr_workgroup_info 0
		.amdhsa_system_vgpr_workitem_id 0
		.amdhsa_next_free_vgpr 92
		.amdhsa_next_free_sgpr 16
		.amdhsa_accum_offset 92
		.amdhsa_reserve_vcc 1
		.amdhsa_float_round_mode_32 0
		.amdhsa_float_round_mode_16_64 0
		.amdhsa_float_denorm_mode_32 3
		.amdhsa_float_denorm_mode_16_64 3
		.amdhsa_dx10_clamp 1
		.amdhsa_ieee_mode 1
		.amdhsa_fp16_overflow 0
		.amdhsa_tg_split 0
		.amdhsa_exception_fp_ieee_invalid_op 0
		.amdhsa_exception_fp_denorm_src 0
		.amdhsa_exception_fp_ieee_div_zero 0
		.amdhsa_exception_fp_ieee_overflow 0
		.amdhsa_exception_fp_ieee_underflow 0
		.amdhsa_exception_fp_ieee_inexact 0
		.amdhsa_exception_int_div_zero 0
	.end_amdhsa_kernel

amdhsa.kernels:
  - .agpr_count:     0
    .args:
      - .actual_access:  read_only
        .address_space:  global
        .offset:         0
        .size:           8
        .value_kind:     global_buffer
      - .actual_access:  read_only
        .address_space:  global
        .offset:         8
        .size:           8
        .value_kind:     global_buffer
      - .actual_access:  read_only
        .address_space:  global
        .offset:         16
        .size:           8
        .value_kind:     global_buffer
      - .actual_access:  write_only
        .address_space:  global
        .offset:         24
        .size:           8
        .value_kind:     global_buffer
      - .actual_access:  write_only
        .address_space:  global
        .offset:         32
        .size:           8
        .value_kind:     global_buffer
      - .actual_access:  write_only
        .address_space:  global
        .offset:         40
        .size:           8
        .value_kind:     global_buffer
      - .actual_access:  read_only
        .address_space:  global
        .offset:         48
        .size:           8
        .value_kind:     global_buffer
      - .actual_access:  read_only
        .address_space:  global
        .offset:         56
        .size:           8
        .value_kind:     global_buffer
      - .actual_access:  read_only
        .address_space:  global
        .offset:         64
        .size:           8
        .value_kind:     global_buffer
      - .actual_access:  write_only
        .address_space:  global
        .offset:         72
        .size:           8
        .value_kind:     global_buffer
    .group_segment_fixed_size: 0
    .kernarg_segment_align: 8
    .kernarg_segment_size: 80
    .language:       OpenCL C
    .language_version:
      - 2
      - 0
    .max_flat_workgroup_size: 256
    .name:           _Z8k_phase1PKfS0_S0_PDv4_jS2_PiS3_P15HIP_vector_typeIiLj2EES0_Pf
    .private_segment_fixed_size: 0
    .sgpr_count:     18
    .sgpr_spill_count: 0
    .symbol:         _Z8k_phase1PKfS0_S0_PDv4_jS2_PiS3_P15HIP_vector_typeIiLj2EES0_Pf.kd
    .uniform_work_group_size: 1
    .uses_dynamic_stack: false
    .vgpr_count:     19
    .vgpr_spill_count: 0
    .wavefront_size: 64
  - .agpr_count:     0
    .args:
      - .actual_access:  read_only
        .address_space:  global
        .offset:         0
        .size:           8
        .value_kind:     global_buffer
      - .actual_access:  read_only
        .address_space:  global
        .offset:         8
        .size:           8
        .value_kind:     global_buffer
      - .actual_access:  read_only
        .address_space:  global
        .offset:         16
        .size:           8
        .value_kind:     global_buffer
      - .actual_access:  read_only
        .address_space:  global
        .offset:         24
        .size:           8
        .value_kind:     global_buffer
      - .address_space:  global
        .offset:         32
        .size:           8
        .value_kind:     global_buffer
      - .actual_access:  write_only
        .address_space:  global
        .offset:         40
        .size:           8
        .value_kind:     global_buffer
      - .actual_access:  write_only
        .address_space:  global
        .offset:         48
        .size:           8
        .value_kind:     global_buffer
      - .actual_access:  write_only
        .address_space:  global
        .offset:         56
        .size:           8
        .value_kind:     global_buffer
      - .actual_access:  read_only
        .address_space:  global
        .offset:         64
        .size:           8
        .value_kind:     global_buffer
      - .actual_access:  write_only
        .address_space:  global
        .offset:         72
        .size:           8
        .value_kind:     global_buffer
      - .actual_access:  write_only
        .address_space:  global
        .offset:         80
        .size:           8
        .value_kind:     global_buffer
    .group_segment_fixed_size: 90112
    .kernarg_segment_align: 8
    .kernarg_segment_size: 88
    .language:       OpenCL C
    .language_version:
      - 2
      - 0
    .max_flat_workgroup_size: 768
    .name:           _Z7k_gemm1PKfS0_PKDv4_jPKiPiS6_P15HIP_vector_typeIiLj2EEPDF16_S0_S6_S9_
    .private_segment_fixed_size: 0
    .sgpr_count:     48
    .sgpr_spill_count: 0
    .symbol:         _Z7k_gemm1PKfS0_PKDv4_jPKiPiS6_P15HIP_vector_typeIiLj2EEPDF16_S0_S6_S9_.kd
    .uniform_work_group_size: 1
    .uses_dynamic_stack: false
    .vgpr_count:     168
    .vgpr_spill_count: 0
    .wavefront_size: 64
  - .agpr_count:     0
    .args:
      - .actual_access:  read_only
        .address_space:  global
        .offset:         0
        .size:           8
        .value_kind:     global_buffer
      - .actual_access:  read_only
        .address_space:  global
        .offset:         8
        .size:           8
        .value_kind:     global_buffer
      - .actual_access:  read_only
        .address_space:  global
        .offset:         16
        .size:           8
        .value_kind:     global_buffer
      - .actual_access:  read_only
        .address_space:  global
        .offset:         24
        .size:           8
        .value_kind:     global_buffer
      - .actual_access:  read_only
        .address_space:  global
        .offset:         32
        .size:           8
        .value_kind:     global_buffer
      - .actual_access:  read_only
        .address_space:  global
        .offset:         40
        .size:           8
        .value_kind:     global_buffer
      - .actual_access:  write_only
        .address_space:  global
        .offset:         48
        .size:           8
        .value_kind:     global_buffer
    .group_segment_fixed_size: 12576
    .kernarg_segment_align: 8
    .kernarg_segment_size: 56
    .language:       OpenCL C
    .language_version:
      - 2
      - 0
    .max_flat_workgroup_size: 256
    .name:           _Z8k_agg1g2PKDv4_jPKiS3_PK15HIP_vector_typeIiLj2EEPKfS1_PDF16_
    .private_segment_fixed_size: 0
    .sgpr_count:     52
    .sgpr_spill_count: 0
    .symbol:         _Z8k_agg1g2PKDv4_jPKiS3_PK15HIP_vector_typeIiLj2EEPKfS1_PDF16_.kd
    .uniform_work_group_size: 1
    .uses_dynamic_stack: false
    .vgpr_count:     126
    .vgpr_spill_count: 0
    .wavefront_size: 64
  - .agpr_count:     0
    .args:
      - .actual_access:  read_only
        .address_space:  global
        .offset:         0
        .size:           8
        .value_kind:     global_buffer
      - .actual_access:  read_only
        .address_space:  global
        .offset:         8
        .size:           8
        .value_kind:     global_buffer
      - .actual_access:  read_only
        .address_space:  global
        .offset:         16
        .size:           8
        .value_kind:     global_buffer
      - .actual_access:  read_only
        .address_space:  global
        .offset:         24
        .size:           8
        .value_kind:     global_buffer
      - .actual_access:  read_only
        .address_space:  global
        .offset:         32
        .size:           8
        .value_kind:     global_buffer
      - .actual_access:  write_only
        .address_space:  global
        .offset:         40
        .size:           8
        .value_kind:     global_buffer
      - .actual_access:  write_only
        .address_space:  global
        .offset:         48
        .size:           8
        .value_kind:     global_buffer
      - .actual_access:  write_only
        .address_space:  global
        .offset:         56
        .size:           8
        .value_kind:     global_buffer
    .group_segment_fixed_size: 0
    .kernarg_segment_align: 8
    .kernarg_segment_size: 64
    .language:       OpenCL C
    .language_version:
      - 2
      - 0
    .max_flat_workgroup_size: 256
    .name:           _Z6k_agg2PKDv4_jPKiS3_PK15HIP_vector_typeIiLj2EEPKfPfSA_PS_
    .private_segment_fixed_size: 0
    .sgpr_count:     18
    .sgpr_spill_count: 0
    .symbol:         _Z6k_agg2PKDv4_jPKiS3_PK15HIP_vector_typeIiLj2EEPKfPfSA_PS_.kd
    .uniform_work_group_size: 1
    .uses_dynamic_stack: false
    .vgpr_count:     62
    .vgpr_spill_count: 0
    .wavefront_size: 64
  - .agpr_count:     0
    .args:
      - .actual_access:  read_only
        .address_space:  global
        .offset:         0
        .size:           8
        .value_kind:     global_buffer
      - .actual_access:  read_only
        .address_space:  global
        .offset:         8
        .size:           8
        .value_kind:     global_buffer
      - .actual_access:  read_only
        .address_space:  global
        .offset:         16
        .size:           8
        .value_kind:     global_buffer
      - .actual_access:  read_only
        .address_space:  global
        .offset:         24
        .size:           8
        .value_kind:     global_buffer
      - .actual_access:  read_only
        .address_space:  global
        .offset:         32
        .size:           8
        .value_kind:     global_buffer
      - .actual_access:  read_only
        .address_space:  global
        .offset:         40
        .size:           8
        .value_kind:     global_buffer
      - .actual_access:  read_only
        .address_space:  global
        .offset:         48
        .size:           8
        .value_kind:     global_buffer
      - .actual_access:  write_only
        .address_space:  global
        .offset:         56
        .size:           8
        .value_kind:     global_buffer
      - .actual_access:  write_only
        .address_space:  global
        .offset:         64
        .size:           8
        .value_kind:     global_buffer
    .group_segment_fixed_size: 22528
    .kernarg_segment_align: 8
    .kernarg_segment_size: 72
    .language:       OpenCL C
    .language_version:
      - 2
      - 0
    .max_flat_workgroup_size: 256
    .name:           _Z9k_readoutPKDv4_jPKfPKiPK15HIP_vector_typeIiLj2EES3_S3_S3_PfSA_
    .private_segment_fixed_size: 0
    .sgpr_count:     22
    .sgpr_spill_count: 0
    .symbol:         _Z9k_readoutPKDv4_jPKfPKiPK15HIP_vector_typeIiLj2EES3_S3_S3_PfSA_.kd
    .uniform_work_group_size: 1
    .uses_dynamic_stack: false
    .vgpr_count:     92
    .vgpr_spill_count: 0
    .wavefront_size: 64
